# speedup vs baseline: 1.0060x; 1.0060x over previous
.LBB1_36:
	s_or_b64 exec, exec, s[2:3]
	s_waitcnt vmcnt(0)
	v_add_f32_e32 v103, 0, v103
	v_add_f32_e32 v103, v103, v104
	v_add_f32_e32 v103, v103, v105
	v_add_f32_e32 v103, v103, v106
	v_add_f32_e32 v103, v103, v107
	v_add_f32_e32 v103, v103, v108
	v_add_f32_e32 v103, v103, v109
	v_add_f32_e32 v103, v103, v110
	v_add_f32_e32 v103, v103, v111
	v_add_f32_e32 v103, v103, v112
	v_add_f32_e32 v103, v103, v113
	v_add_f32_e32 v103, v103, v114
	v_add_f32_e32 v103, v103, v115
	v_add_f32_e32 v103, v103, v116
	v_add_f32_e32 v103, v103, v117
	v_add_f32_e32 v103, v103, v118
	v_add_f32_e32 v103, v103, v119
	v_add_f32_e32 v103, v103, v120
	v_add_f32_e32 v103, v103, v121
	v_add_f32_e32 v103, v103, v122
	s_mov_b32 s14, 0xf800000
	s_mov_b32 s11, 0x41e6d4ca
	v_cmp_gt_f32_e32 vcc, s14, v103
	v_mul_f32_e32 v104, 0x4f800000, v103
	s_nop 0
	v_cndmask_b32_e32 v104, v103, v104, vcc
	v_sqrt_f32_e32 v103, v104
	s_nop 0
	v_add_u32_e32 v105, -1, v103
	v_fma_f32 v108, -v105, v103, v104
	v_cmp_ge_f32_e64 s[2:3], 0, v108
	v_add_u32_e32 v108, 1, v103
	s_nop 0
	v_cndmask_b32_e64 v105, v103, v105, s[2:3]
	v_fma_f32 v103, -v108, v103, v104
	v_cmp_lt_f32_e64 s[2:3], 0, v103
	s_nop 1
	v_cndmask_b32_e64 v103, v105, v108, s[2:3]
	v_mul_f32_e32 v105, 0x37800000, v103
	v_cndmask_b32_e32 v105, v103, v105, vcc
	v_mov_b32_e32 v103, 0x260
	v_cmp_class_f32_e32 vcc, v104, v103
	s_nop 1
	v_cndmask_b32_e32 v104, v105, v104, vcc
	v_add_f32_e32 v104, 0x322bcc77, v104
	v_div_scale_f32 v108, s[2:3], v104, v104, s11
	v_rcp_f32_e32 v105, v108
	s_nop 0
	v_fma_f32 v109, -v108, v105, 1.0
	v_fmac_f32_e32 v105, v109, v105
	v_div_scale_f32 v107, vcc, s11, v104, s11
	v_mul_f32_e32 v106, v107, v105
	v_fma_f32 v111, -v108, v106, v107
	v_fmac_f32_e32 v106, v111, v105
	v_fma_f32 v107, -v108, v106, v107
	s_nop 0
	v_div_fmas_f32 v109, v107, v105, v106
	v_div_fixup_f32 v109, v109, v104, s11
	v_lshlrev_b32_e32 v110, 2, v101
	ds_bpermute_b32 v108, v110, v109
	ds_bpermute_b32 v111, v110, v109 offset:64
	ds_bpermute_b32 v112, v110, v109 offset:128
	ds_bpermute_b32 v113, v110, v109 offset:192
	s_mul_i32 s2, s23, 0x1f80
	s_add_i32 s6, s8, s2
	s_movk_i32 s2, 0x88
	v_and_b32_e32 v66, 0x70, v100
	v_add_u32_e32 v71, s10, v66
	v_lshrrev_b32_e32 v67, 4, v100
	v_lshlrev_b32_e32 v67, 3, v67
	v_add_u32_e32 v72, s6, v67
	s_mov_b32 s34, 0x3d0df4e0
	v_mad_u32_u24 v120, v101, s2, v72
	ds_read_b128 v[114:117], v71 offset:8832
	s_waitcnt lgkmcnt(0)
	v_mul_f32_e32 v64, v114, v108
	v_mul_f32_e32 v65, v115, v108
	v_mul_f32_e32 v66, v116, v108
	v_mul_f32_e32 v67, v117, v108
	v_fmaak_f32 v60, v60, v64, 0xc1e6d4ca
	v_fmaak_f32 v61, v61, v65, 0xc1e6d4ca
	v_fmaak_f32 v62, v62, v66, 0xc1e6d4ca
	v_fmaak_f32 v63, v63, v67, 0xc1e6d4ca
	v_exp_f32_e32 v64, v60
	v_exp_f32_e32 v65, v61
	v_exp_f32_e32 v66, v62
	v_exp_f32_e32 v67, v63
	v_fma_f32 v60, v60, s34, 1.0
	v_fma_f32 v61, v61, s34, 1.0
	v_fma_f32 v62, v62, s34, 1.0
	v_fma_f32 v63, v63, s34, 1.0
	v_mul_f32_e32 v60, v64, v60
	v_mul_f32_e32 v61, v65, v61
	v_mul_f32_e32 v62, v66, v62
	v_mul_f32_e32 v63, v67, v63
	v_cvt_pk_bf16_f32 v68, v64, v65
	v_cvt_pk_bf16_f32 v69, v66, v67
	ds_write_b64 v120, v[68:69] offset:10240
	v_cvt_pk_bf16_f32 v72, v60, v61
	v_cvt_pk_bf16_f32 v73, v62, v63
	v_mul_f32_e32 v64, v114, v111
	v_mul_f32_e32 v65, v115, v111
	v_mul_f32_e32 v66, v116, v111
	v_mul_f32_e32 v67, v117, v111
	v_fmaak_f32 v56, v56, v64, 0xc1e6d4ca
	v_fmaak_f32 v57, v57, v65, 0xc1e6d4ca
	v_fmaak_f32 v58, v58, v66, 0xc1e6d4ca
	v_fmaak_f32 v59, v59, v67, 0xc1e6d4ca
	v_exp_f32_e32 v64, v56
	v_exp_f32_e32 v65, v57
	v_exp_f32_e32 v66, v58
	v_exp_f32_e32 v67, v59
	v_fma_f32 v56, v56, s34, 1.0
	v_fma_f32 v57, v57, s34, 1.0
	v_fma_f32 v58, v58, s34, 1.0
	v_fma_f32 v59, v59, s34, 1.0
	v_mul_f32_e32 v56, v64, v56
	v_mul_f32_e32 v57, v65, v57
	v_mul_f32_e32 v58, v66, v58
	v_mul_f32_e32 v59, v67, v59
	v_cvt_pk_bf16_f32 v68, v64, v65
	v_cvt_pk_bf16_f32 v69, v66, v67
	ds_write_b64 v120, v[68:69] offset:12416
	v_cvt_pk_bf16_f32 v74, v56, v57
	v_cvt_pk_bf16_f32 v75, v58, v59
	v_mul_f32_e32 v64, v114, v112
	v_mul_f32_e32 v65, v115, v112
	v_mul_f32_e32 v66, v116, v112
	v_mul_f32_e32 v67, v117, v112
	v_fmaak_f32 v52, v52, v64, 0xc1e6d4ca
	v_fmaak_f32 v53, v53, v65, 0xc1e6d4ca
	v_fmaak_f32 v54, v54, v66, 0xc1e6d4ca
	v_fmaak_f32 v55, v55, v67, 0xc1e6d4ca
	v_exp_f32_e32 v64, v52
	v_exp_f32_e32 v65, v53
	v_exp_f32_e32 v66, v54
	v_exp_f32_e32 v67, v55
	v_fma_f32 v52, v52, s34, 1.0
	v_fma_f32 v53, v53, s34, 1.0
	v_fma_f32 v54, v54, s34, 1.0
	v_fma_f32 v55, v55, s34, 1.0
	v_mul_f32_e32 v52, v64, v52
	v_mul_f32_e32 v53, v65, v53
	v_mul_f32_e32 v54, v66, v54
	v_mul_f32_e32 v55, v67, v55
	v_cvt_pk_bf16_f32 v68, v64, v65
	v_cvt_pk_bf16_f32 v69, v66, v67
	ds_write_b64 v120, v[68:69] offset:14592
	v_cvt_pk_bf16_f32 v76, v52, v53
	v_cvt_pk_bf16_f32 v77, v54, v55
	v_mul_f32_e32 v64, v114, v113
	v_mul_f32_e32 v65, v115, v113
	v_mul_f32_e32 v66, v116, v113
	v_mul_f32_e32 v67, v117, v113
	ds_read_b128 v[114:117], v71 offset:8896
	v_fmaak_f32 v48, v48, v64, 0xc1e6d4ca
	v_fmaak_f32 v49, v49, v65, 0xc1e6d4ca
	v_fmaak_f32 v50, v50, v66, 0xc1e6d4ca
	v_fmaak_f32 v51, v51, v67, 0xc1e6d4ca
	v_exp_f32_e32 v64, v48
	v_exp_f32_e32 v65, v49
	v_exp_f32_e32 v66, v50
	v_exp_f32_e32 v67, v51
	v_fma_f32 v48, v48, s34, 1.0
	v_fma_f32 v49, v49, s34, 1.0
	v_fma_f32 v50, v50, s34, 1.0
	v_fma_f32 v51, v51, s34, 1.0
	v_mul_f32_e32 v48, v64, v48
	v_mul_f32_e32 v49, v65, v49
	v_mul_f32_e32 v50, v66, v50
	v_mul_f32_e32 v51, v67, v51
	v_cvt_pk_bf16_f32 v68, v64, v65
	v_cvt_pk_bf16_f32 v69, v66, v67
	ds_write_b64 v120, v[68:69] offset:16768
	v_cvt_pk_bf16_f32 v78, v48, v49
	v_cvt_pk_bf16_f32 v79, v50, v51
	s_waitcnt lgkmcnt(0)
	v_mul_f32_e32 v64, v114, v108
	v_mul_f32_e32 v65, v115, v108
	v_mul_f32_e32 v66, v116, v108
	v_mul_f32_e32 v67, v117, v108
	v_fmaak_f32 v44, v44, v64, 0xc1e6d4ca
	v_fmaak_f32 v45, v45, v65, 0xc1e6d4ca
	v_fmaak_f32 v46, v46, v66, 0xc1e6d4ca
	v_fmaak_f32 v47, v47, v67, 0xc1e6d4ca
	v_exp_f32_e32 v64, v44
	v_exp_f32_e32 v65, v45
	v_exp_f32_e32 v66, v46
	v_exp_f32_e32 v67, v47
	v_fma_f32 v44, v44, s34, 1.0
	v_fma_f32 v45, v45, s34, 1.0
	v_fma_f32 v46, v46, s34, 1.0
	v_fma_f32 v47, v47, s34, 1.0
	v_mul_f32_e32 v44, v64, v44
	v_mul_f32_e32 v45, v65, v45
	v_mul_f32_e32 v46, v66, v46
	v_mul_f32_e32 v47, v67, v47
	v_cvt_pk_bf16_f32 v68, v64, v65
	v_cvt_pk_bf16_f32 v69, v66, v67
	ds_write_b64 v120, v[68:69] offset:10272
	v_cvt_pk_bf16_f32 v80, v44, v45
	v_cvt_pk_bf16_f32 v81, v46, v47
	v_mul_f32_e32 v64, v114, v111
	v_mul_f32_e32 v65, v115, v111
	v_mul_f32_e32 v66, v116, v111
	v_mul_f32_e32 v67, v117, v111
	v_fmaak_f32 v40, v40, v64, 0xc1e6d4ca
	v_fmaak_f32 v41, v41, v65, 0xc1e6d4ca
	v_fmaak_f32 v42, v42, v66, 0xc1e6d4ca
	v_fmaak_f32 v43, v43, v67, 0xc1e6d4ca
	v_exp_f32_e32 v64, v40
	v_exp_f32_e32 v65, v41
	v_exp_f32_e32 v66, v42
	v_exp_f32_e32 v67, v43
	v_fma_f32 v40, v40, s34, 1.0
	v_fma_f32 v41, v41, s34, 1.0
	v_fma_f32 v42, v42, s34, 1.0
	v_fma_f32 v43, v43, s34, 1.0
	v_mul_f32_e32 v40, v64, v40
	v_mul_f32_e32 v41, v65, v41
	v_mul_f32_e32 v42, v66, v42
	v_mul_f32_e32 v43, v67, v43
	v_cvt_pk_bf16_f32 v68, v64, v65
	v_cvt_pk_bf16_f32 v69, v66, v67
	ds_write_b64 v120, v[68:69] offset:12448
	v_cvt_pk_bf16_f32 v82, v40, v41
	v_cvt_pk_bf16_f32 v83, v42, v43
	v_mul_f32_e32 v64, v114, v112
	v_mul_f32_e32 v65, v115, v112
	v_mul_f32_e32 v66, v116, v112
	v_mul_f32_e32 v67, v117, v112
	v_fmaak_f32 v36, v36, v64, 0xc1e6d4ca
	v_fmaak_f32 v37, v37, v65, 0xc1e6d4ca
	v_fmaak_f32 v38, v38, v66, 0xc1e6d4ca
	v_fmaak_f32 v39, v39, v67, 0xc1e6d4ca
	v_exp_f32_e32 v64, v36
	v_exp_f32_e32 v65, v37
	v_exp_f32_e32 v66, v38
	v_exp_f32_e32 v67, v39
	v_fma_f32 v36, v36, s34, 1.0
	v_fma_f32 v37, v37, s34, 1.0
	v_fma_f32 v38, v38, s34, 1.0
	v_fma_f32 v39, v39, s34, 1.0
	v_mul_f32_e32 v36, v64, v36
	v_mul_f32_e32 v37, v65, v37
	v_mul_f32_e32 v38, v66, v38
	v_mul_f32_e32 v39, v67, v39
	v_cvt_pk_bf16_f32 v68, v64, v65
	v_cvt_pk_bf16_f32 v69, v66, v67
	ds_write_b64 v120, v[68:69] offset:14624
	v_cvt_pk_bf16_f32 v84, v36, v37
	v_cvt_pk_bf16_f32 v85, v38, v39
	v_mul_f32_e32 v64, v114, v113
	v_mul_f32_e32 v65, v115, v113
	v_mul_f32_e32 v66, v116, v113
	v_mul_f32_e32 v67, v117, v113
	ds_read_b128 v[114:117], v71 offset:8960
	v_fmaak_f32 v32, v32, v64, 0xc1e6d4ca
	v_fmaak_f32 v33, v33, v65, 0xc1e6d4ca
	v_fmaak_f32 v34, v34, v66, 0xc1e6d4ca
	v_fmaak_f32 v35, v35, v67, 0xc1e6d4ca
	v_exp_f32_e32 v64, v32
	v_exp_f32_e32 v65, v33
	v_exp_f32_e32 v66, v34
	v_exp_f32_e32 v67, v35
	v_fma_f32 v32, v32, s34, 1.0
	v_fma_f32 v33, v33, s34, 1.0
	v_fma_f32 v34, v34, s34, 1.0
	v_fma_f32 v35, v35, s34, 1.0
	v_mul_f32_e32 v32, v64, v32
	v_mul_f32_e32 v33, v65, v33
	v_mul_f32_e32 v34, v66, v34
	v_mul_f32_e32 v35, v67, v35
	v_cvt_pk_bf16_f32 v68, v64, v65
	v_cvt_pk_bf16_f32 v69, v66, v67
	ds_write_b64 v120, v[68:69] offset:16800
	v_cvt_pk_bf16_f32 v86, v32, v33
	v_cvt_pk_bf16_f32 v87, v34, v35
	s_waitcnt lgkmcnt(0)
	v_mul_f32_e32 v64, v114, v108
	v_mul_f32_e32 v65, v115, v108
	v_mul_f32_e32 v66, v116, v108
	v_mul_f32_e32 v67, v117, v108
	v_fmaak_f32 v28, v28, v64, 0xc1e6d4ca
	v_fmaak_f32 v29, v29, v65, 0xc1e6d4ca
	v_fmaak_f32 v30, v30, v66, 0xc1e6d4ca
	v_fmaak_f32 v31, v31, v67, 0xc1e6d4ca
	v_exp_f32_e32 v64, v28
	v_exp_f32_e32 v65, v29
	v_exp_f32_e32 v66, v30
	v_exp_f32_e32 v67, v31
	v_fma_f32 v28, v28, s34, 1.0
	v_fma_f32 v29, v29, s34, 1.0
	v_fma_f32 v30, v30, s34, 1.0
	v_fma_f32 v31, v31, s34, 1.0
	v_mul_f32_e32 v28, v64, v28
	v_mul_f32_e32 v29, v65, v29
	v_mul_f32_e32 v30, v66, v30
	v_mul_f32_e32 v31, v67, v31
	v_cvt_pk_bf16_f32 v68, v64, v65
	v_cvt_pk_bf16_f32 v69, v66, v67
	ds_write_b64 v120, v[68:69] offset:10304
	v_cvt_pk_bf16_f32 v88, v28, v29
	v_cvt_pk_bf16_f32 v89, v30, v31
	v_mul_f32_e32 v64, v114, v111
	v_mul_f32_e32 v65, v115, v111
	v_mul_f32_e32 v66, v116, v111
	v_mul_f32_e32 v67, v117, v111
	v_fmaak_f32 v24, v24, v64, 0xc1e6d4ca
	v_fmaak_f32 v25, v25, v65, 0xc1e6d4ca
	v_fmaak_f32 v26, v26, v66, 0xc1e6d4ca
	v_fmaak_f32 v27, v27, v67, 0xc1e6d4ca
	v_exp_f32_e32 v64, v24
	v_exp_f32_e32 v65, v25
	v_exp_f32_e32 v66, v26
	v_exp_f32_e32 v67, v27
	v_fma_f32 v24, v24, s34, 1.0
	v_fma_f32 v25, v25, s34, 1.0
	v_fma_f32 v26, v26, s34, 1.0
	v_fma_f32 v27, v27, s34, 1.0
	v_mul_f32_e32 v24, v64, v24
	v_mul_f32_e32 v25, v65, v25
	v_mul_f32_e32 v26, v66, v26
	v_mul_f32_e32 v27, v67, v27
	v_cvt_pk_bf16_f32 v68, v64, v65
	v_cvt_pk_bf16_f32 v69, v66, v67
	ds_write_b64 v120, v[68:69] offset:12480
	v_cvt_pk_bf16_f32 v90, v24, v25
	v_cvt_pk_bf16_f32 v91, v26, v27
	v_mul_f32_e32 v64, v114, v112
	v_mul_f32_e32 v65, v115, v112
	v_mul_f32_e32 v66, v116, v112
	v_mul_f32_e32 v67, v117, v112
	v_fmaak_f32 v20, v20, v64, 0xc1e6d4ca
	v_fmaak_f32 v21, v21, v65, 0xc1e6d4ca
	v_fmaak_f32 v22, v22, v66, 0xc1e6d4ca
	v_fmaak_f32 v23, v23, v67, 0xc1e6d4ca
	v_exp_f32_e32 v64, v20
	v_exp_f32_e32 v65, v21
	v_exp_f32_e32 v66, v22
	v_exp_f32_e32 v67, v23
	v_fma_f32 v20, v20, s34, 1.0
	v_fma_f32 v21, v21, s34, 1.0
	v_fma_f32 v22, v22, s34, 1.0
	v_fma_f32 v23, v23, s34, 1.0
	v_mul_f32_e32 v20, v64, v20
	v_mul_f32_e32 v21, v65, v21
	v_mul_f32_e32 v22, v66, v22
	v_mul_f32_e32 v23, v67, v23
	v_cvt_pk_bf16_f32 v68, v64, v65
	v_cvt_pk_bf16_f32 v69, v66, v67
	ds_write_b64 v120, v[68:69] offset:14656
	v_cvt_pk_bf16_f32 v92, v20, v21
	v_cvt_pk_bf16_f32 v93, v22, v23
	v_mul_f32_e32 v64, v114, v113
	v_mul_f32_e32 v65, v115, v113
	v_mul_f32_e32 v66, v116, v113
	v_mul_f32_e32 v67, v117, v113
	ds_read_b128 v[114:117], v71 offset:9024
	v_fmaak_f32 v16, v16, v64, 0xc1e6d4ca
	v_fmaak_f32 v17, v17, v65, 0xc1e6d4ca
	v_fmaak_f32 v18, v18, v66, 0xc1e6d4ca
	v_fmaak_f32 v19, v19, v67, 0xc1e6d4ca
	v_exp_f32_e32 v64, v16
	v_exp_f32_e32 v65, v17
	v_exp_f32_e32 v66, v18
	v_exp_f32_e32 v67, v19
	v_fma_f32 v16, v16, s34, 1.0
	v_fma_f32 v17, v17, s34, 1.0
	v_fma_f32 v18, v18, s34, 1.0
	v_fma_f32 v19, v19, s34, 1.0
	v_mul_f32_e32 v16, v64, v16
	v_mul_f32_e32 v17, v65, v17
	v_mul_f32_e32 v18, v66, v18
	v_mul_f32_e32 v19, v67, v19
	v_cvt_pk_bf16_f32 v68, v64, v65
	v_cvt_pk_bf16_f32 v69, v66, v67
	ds_write_b64 v120, v[68:69] offset:16832
	v_cvt_pk_bf16_f32 v94, v16, v17
	v_cvt_pk_bf16_f32 v95, v18, v19
	s_waitcnt lgkmcnt(0)
	v_mul_f32_e32 v64, v114, v108
	v_mul_f32_e32 v65, v115, v108
	v_mul_f32_e32 v66, v116, v108
	v_mul_f32_e32 v67, v117, v108
	v_fmaak_f32 v12, v12, v64, 0xc1e6d4ca
	v_fmaak_f32 v13, v13, v65, 0xc1e6d4ca
	v_fmaak_f32 v14, v14, v66, 0xc1e6d4ca
	v_fmaak_f32 v15, v15, v67, 0xc1e6d4ca
	v_exp_f32_e32 v64, v12
	v_exp_f32_e32 v65, v13
	v_exp_f32_e32 v66, v14
	v_exp_f32_e32 v67, v15
	v_fma_f32 v12, v12, s34, 1.0
	v_fma_f32 v13, v13, s34, 1.0
	v_fma_f32 v14, v14, s34, 1.0
	v_fma_f32 v15, v15, s34, 1.0
	v_mul_f32_e32 v12, v64, v12
	v_mul_f32_e32 v13, v65, v13
	v_mul_f32_e32 v14, v66, v14
	v_mul_f32_e32 v15, v67, v15
	v_cvt_pk_bf16_f32 v68, v64, v65
	v_cvt_pk_bf16_f32 v69, v66, v67
	ds_write_b64 v120, v[68:69] offset:10336
	v_cvt_pk_bf16_f32 v96, v12, v13
	v_cvt_pk_bf16_f32 v97, v14, v15
	v_mul_f32_e32 v64, v114, v111
	v_mul_f32_e32 v65, v115, v111
	v_mul_f32_e32 v66, v116, v111
	v_mul_f32_e32 v67, v117, v111
	v_fmaak_f32 v8, v8, v64, 0xc1e6d4ca
	v_fmaak_f32 v9, v9, v65, 0xc1e6d4ca
	v_fmaak_f32 v10, v10, v66, 0xc1e6d4ca
	v_fmaak_f32 v11, v11, v67, 0xc1e6d4ca
	v_exp_f32_e32 v64, v8
	v_exp_f32_e32 v65, v9
	v_exp_f32_e32 v66, v10
	v_exp_f32_e32 v67, v11
	v_fma_f32 v8, v8, s34, 1.0
	v_fma_f32 v9, v9, s34, 1.0
	v_fma_f32 v10, v10, s34, 1.0
	v_fma_f32 v11, v11, s34, 1.0
	v_mul_f32_e32 v8, v64, v8
	v_mul_f32_e32 v9, v65, v9
	v_mul_f32_e32 v10, v66, v10
	v_mul_f32_e32 v11, v67, v11
	v_cvt_pk_bf16_f32 v68, v64, v65
	v_cvt_pk_bf16_f32 v69, v66, v67
	ds_write_b64 v120, v[68:69] offset:12512
	v_cvt_pk_bf16_f32 v98, v8, v9
	v_cvt_pk_bf16_f32 v99, v10, v11
	v_mul_f32_e32 v64, v114, v112
	v_mul_f32_e32 v65, v115, v112
	v_mul_f32_e32 v66, v116, v112
	v_mul_f32_e32 v67, v117, v112
	v_fmaak_f32 v4, v4, v64, 0xc1e6d4ca
	v_fmaak_f32 v5, v5, v65, 0xc1e6d4ca
	v_fmaak_f32 v6, v6, v66, 0xc1e6d4ca
	v_fmaak_f32 v7, v7, v67, 0xc1e6d4ca
	v_exp_f32_e32 v64, v4
	v_exp_f32_e32 v65, v5
	v_exp_f32_e32 v66, v6
	v_exp_f32_e32 v67, v7
	v_fma_f32 v4, v4, s34, 1.0
	v_fma_f32 v5, v5, s34, 1.0
	v_fma_f32 v6, v6, s34, 1.0
	v_fma_f32 v7, v7, s34, 1.0
	v_mul_f32_e32 v4, v64, v4
	v_mul_f32_e32 v5, v65, v5
	v_mul_f32_e32 v6, v66, v6
	v_mul_f32_e32 v7, v67, v7
	v_cvt_pk_bf16_f32 v68, v64, v65
	v_cvt_pk_bf16_f32 v69, v66, v67
	ds_write_b64 v120, v[68:69] offset:14688
	v_cvt_pk_bf16_f32 v104, v4, v5
	v_cvt_pk_bf16_f32 v105, v6, v7
	v_mul_f32_e32 v64, v114, v113
	v_mul_f32_e32 v65, v115, v113
	v_mul_f32_e32 v66, v116, v113
	v_mul_f32_e32 v67, v117, v113
	v_fmaak_f32 v0, v0, v64, 0xc1e6d4ca
	v_fmaak_f32 v1, v1, v65, 0xc1e6d4ca
	v_fmaak_f32 v2, v2, v66, 0xc1e6d4ca
	v_fmaak_f32 v3, v3, v67, 0xc1e6d4ca
	v_exp_f32_e32 v64, v0
	v_exp_f32_e32 v65, v1
	v_exp_f32_e32 v66, v2
	v_exp_f32_e32 v67, v3
	v_fma_f32 v0, v0, s34, 1.0
	v_fma_f32 v1, v1, s34, 1.0
	v_fma_f32 v2, v2, s34, 1.0
	v_fma_f32 v3, v3, s34, 1.0
	v_mul_f32_e32 v0, v64, v0
	v_mul_f32_e32 v1, v65, v1
	v_mul_f32_e32 v2, v66, v2
	v_mul_f32_e32 v3, v67, v3
	v_cvt_pk_bf16_f32 v68, v64, v65
	v_cvt_pk_bf16_f32 v69, v66, v67
	ds_write_b64 v120, v[68:69] offset:16864
	v_cvt_pk_bf16_f32 v106, v0, v1
	v_cvt_pk_bf16_f32 v107, v2, v3
	s_movk_i32 s34, 0x88
	v_and_b32_e32 v64, 32, v100
	v_and_b32_e32 v66, 16, v100
	v_mad_u32_u24 v65, v101, s34, v64
	v_add_u32_e32 v65, s6, v65
	v_add_u32_e32 v67, v65, v66
	v_sub_u32_e32 v65, v65, v66
	v_lshrrev_b32_e32 v68, 1, v100
	v_and_b32_e32 v68, 16, v68
	v_bfe_u32 v69, v100, 2, 2
	v_or_b32_e32 v68, v68, v69
	v_and_b32_e32 v69, 3, v100
	v_lshlrev_b32_e32 v69, 3, v69
	v_mad_u32_u24 v68, v68, s34, v69
	v_add_u32_e32 v68, s6, v68
	s_movk_i32 s35, 0x44
	v_mul_u32_u24_e32 v66, s35, v66
	v_add_u32_e32 v69, v68, v66
	v_sub_u32_e32 v68, v68, v66
	ds_read_b64 v[0:1], v67 offset:10240
	ds_read_b64 v[2:3], v65 offset:10264
	ds_read_b64 v[4:5], v67 offset:10304
	ds_read_b64 v[6:7], v65 offset:10328
	ds_read_b64 v[8:9], v67 offset:12424
	ds_read_b64 v[10:11], v67 offset:12416
	ds_read_b64 v[12:13], v67 offset:12488
	ds_read_b64 v[14:15], v67 offset:12480
	ds_read_b64 v[16:17], v65 offset:14608
	ds_read_b64 v[18:19], v67 offset:14600
	ds_read_b64 v[20:21], v65 offset:14672
	ds_read_b64 v[22:23], v67 offset:14664
	ds_read_b64 v[24:25], v65 offset:16792
	ds_read_b64 v[26:27], v65 offset:16784
	ds_read_b64 v[28:29], v65 offset:16856
	ds_read_b64 v[30:31], v65 offset:16848
	ds_read_b64_tr_b16 v[32:33], v69 offset:10240
	ds_read_b64_tr_b16 v[34:35], v68 offset:11872
	ds_read_b64_tr_b16 v[36:37], v69 offset:14592
	ds_read_b64_tr_b16 v[38:39], v68 offset:16224
	ds_read_b64_tr_b16 v[40:41], v69 offset:10816
	ds_read_b64_tr_b16 v[42:43], v69 offset:10272
	ds_read_b64_tr_b16 v[44:45], v69 offset:15168
	ds_read_b64_tr_b16 v[46:47], v69 offset:14624
	ds_read_b64_tr_b16 v[48:49], v68 offset:11392
	ds_read_b64_tr_b16 v[50:51], v69 offset:10848
	ds_read_b64_tr_b16 v[52:53], v68 offset:15744
	ds_read_b64_tr_b16 v[54:55], v69 offset:15200
	ds_read_b64_tr_b16 v[56:57], v68 offset:11968
	ds_read_b64_tr_b16 v[58:59], v68 offset:11424
	ds_read_b64_tr_b16 v[60:61], v68 offset:16320
	ds_read_b64_tr_b16 v[62:63], v68 offset:15776
	ds_read2st64_b32 v[116:117], v102 offset0:22 offset1:23
	s_waitcnt lgkmcnt(0)
	ds_write_b64 v120, v[72:73] offset:10240
	ds_write_b64 v120, v[74:75] offset:12416
	ds_write_b64 v120, v[76:77] offset:14592
	ds_write_b64 v120, v[78:79] offset:16768
	ds_write_b64 v120, v[80:81] offset:10272
	ds_write_b64 v120, v[82:83] offset:12448
	ds_write_b64 v120, v[84:85] offset:14624
	ds_write_b64 v120, v[86:87] offset:16800
	ds_write_b64 v120, v[88:89] offset:10304
	ds_write_b64 v120, v[90:91] offset:12480
	ds_write_b64 v120, v[92:93] offset:14656
	ds_write_b64 v120, v[94:95] offset:16832
	ds_write_b64 v120, v[96:97] offset:10336
	ds_write_b64 v120, v[98:99] offset:12512
	ds_write_b64 v120, v[104:105] offset:14688
	ds_write_b64 v120, v[106:107] offset:16864
	v_and_b32_e32 v110, 1, v100
	v_cmp_eq_u32_e32 vcc, 0, v110
	v_mov_b32_e32 v110, 0xeeeeeeee
	v_mov_b32_e32 v111, 0x44444444
	s_mov_b32 s32, 0x2b8cbccc
	s_mov_b32 s33, 0
	v_cndmask_b32_e32 v64, v110, v111, vcc
	v_mov_b32_e32 v68, 0x3f803f80
	v_mov_b32_e32 v69, v68
	v_mov_b32_e32 v70, v68
	v_mov_b32_e32 v71, v68
	v_mov_b64_e32 v[72:73], s[32:33]
	v_mov_b64_e32 v[76:77], s[32:33]
	v_mov_b64_e32 v[80:81], s[32:33]
	v_mov_b64_e32 v[84:85], s[32:33]
	v_mov_b64_e32 v[88:89], s[32:33]
	v_mov_b64_e32 v[92:93], s[32:33]
	v_mov_b64_e32 v[96:97], s[32:33]
	v_mov_b64_e32 v[104:105], s[32:33]
	s_movk_i32 s30, 100
	v_mov_b32_e32 v122, 0
	v_mov_b32_e32 v121, 0
	s_waitcnt lgkmcnt(0)
	v_mov_b32_dpp v112, v116 quad_perm:[0,2,0,2] row_mask:0xf bank_mask:0xf
	v_mov_b32_dpp v113, v116 quad_perm:[1,3,1,3] row_mask:0xf bank_mask:0xf
	v_mov_b32_dpp v114, v117 quad_perm:[0,2,0,2] row_mask:0xf bank_mask:0xf
	v_mov_b32_dpp v115, v117 quad_perm:[1,3,1,3] row_mask:0xf bank_mask:0xf
	v_smfmac_f32_16x16x64_bf16 v[72:75], v[68:71], v[0:7], v64
	v_smfmac_f32_16x16x64_bf16 v[76:79], v[68:71], v[8:15], v64
	v_smfmac_f32_16x16x64_bf16 v[80:83], v[68:71], v[16:23], v64
	v_smfmac_f32_16x16x64_bf16 v[84:87], v[68:71], v[24:31], v64
	s_nop 4
.Lsk_loop:
	v_add_f32_dpp v108, v72, v73 quad_perm:[0,1,2,3] row_mask:0x1 bank_mask:0xf
	v_add_f32_dpp v108, v76, v77 quad_perm:[0,1,2,3] row_mask:0x2 bank_mask:0xf
	v_add_f32_dpp v108, v80, v81 quad_perm:[0,1,2,3] row_mask:0x4 bank_mask:0xf
	v_add_f32_dpp v108, v84, v85 quad_perm:[0,1,2,3] row_mask:0x8 bank_mask:0xf
	v_rcp_f32_e32 v109, v108
	v_mov_b64_e32 v[88:89], s[32:33]
	v_mov_b64_e32 v[92:93], s[32:33]
	v_mul_f32_dpp v110, v109, v114 quad_perm:[0,2,0,2] row_mask:0xf bank_mask:0xf
	v_mul_f32_dpp v111, v109, v115 quad_perm:[1,3,1,3] row_mask:0xf bank_mask:0xf
	v_cvt_pk_bf16_f32 v68, v110, v111
	v_mov_b64_e32 v[96:97], s[32:33]
	v_mov_b64_e32 v[104:105], s[32:33]
	v_mov_b32_dpp v69, v68 row_ror:4 row_mask:0xf bank_mask:0xf
	v_mov_b32_dpp v70, v68 row_ror:8 row_mask:0xf bank_mask:0xf
	v_mov_b32_dpp v71, v68 row_ror:12 row_mask:0xf bank_mask:0xf
	s_nop 1
	v_smfmac_f32_16x16x64_bf16 v[88:91], v[68:71], v[32:39], v64
	v_smfmac_f32_16x16x64_bf16 v[92:95], v[68:71], v[40:47], v64
	v_smfmac_f32_16x16x64_bf16 v[96:99], v[68:71], v[48:55], v64
	v_smfmac_f32_16x16x64_bf16 v[104:107], v[68:71], v[56:63], v64
	s_nop 4
	v_add_f32_dpp v108, v88, v89 quad_perm:[0,1,2,3] row_mask:0x1 bank_mask:0xf
	v_add_f32_dpp v108, v92, v93 quad_perm:[0,1,2,3] row_mask:0x2 bank_mask:0xf
	v_add_f32_dpp v108, v96, v97 quad_perm:[0,1,2,3] row_mask:0x4 bank_mask:0xf
	v_add_f32_dpp v108, v104, v105 quad_perm:[0,1,2,3] row_mask:0x8 bank_mask:0xf
	v_rcp_f32_e32 v109, v108
	v_mov_b64_e32 v[72:73], s[32:33]
	v_mov_b64_e32 v[76:77], s[32:33]
	v_mul_f32_dpp v110, v109, v112 quad_perm:[0,2,0,2] row_mask:0xf bank_mask:0xf
	v_mul_f32_dpp v111, v109, v113 quad_perm:[1,3,1,3] row_mask:0xf bank_mask:0xf
	v_cvt_pk_bf16_f32 v68, v110, v111
	v_mov_b64_e32 v[80:81], s[32:33]
	v_mov_b64_e32 v[84:85], s[32:33]
	v_mov_b32_dpp v69, v68 row_ror:4 row_mask:0xf bank_mask:0xf
	v_mov_b32_dpp v70, v68 row_ror:8 row_mask:0xf bank_mask:0xf
	v_mov_b32_dpp v71, v68 row_ror:12 row_mask:0xf bank_mask:0xf
	s_nop 1
	v_smfmac_f32_16x16x64_bf16 v[72:75], v[68:71], v[0:7], v64
	v_smfmac_f32_16x16x64_bf16 v[76:79], v[68:71], v[8:15], v64
	v_smfmac_f32_16x16x64_bf16 v[80:83], v[68:71], v[16:23], v64
	v_smfmac_f32_16x16x64_bf16 v[84:87], v[68:71], v[24:31], v64
	v_cmp_ne_u32_e32 vcc, v68, v122
	v_cmp_ne_u32_e64 s[36:37], v68, v121
	v_mov_b32_e32 v121, v122
	v_mov_b32_e32 v122, v68
	s_cmp_eq_u64 vcc, 0
	s_cselect_b32 s30, 1, s30
	s_add_i32 s38, s30, -1
	s_and_b32 s38, s38, 1
	s_add_i32 s38, s38, 1
	s_cmp_eq_u64 s[36:37], 0
	s_cselect_b32 s30, s38, s30
	s_add_i32 s30, s30, -1
	s_cmp_lg_u32 s30, 0
	s_cbranch_scc1 .Lsk_loop
	v_add_f32_dpp v108, v72, v73 quad_perm:[0,1,2,3] row_mask:0x1 bank_mask:0xf
	v_add_f32_dpp v108, v76, v77 quad_perm:[0,1,2,3] row_mask:0x2 bank_mask:0xf
	v_add_f32_dpp v108, v80, v81 quad_perm:[0,1,2,3] row_mask:0x4 bank_mask:0xf
	v_add_f32_dpp v108, v84, v85 quad_perm:[0,1,2,3] row_mask:0x8 bank_mask:0xf
	v_rcp_f32_e32 v109, v108
	s_mov_b32 s34, 0x3d0df4e0
	s_mov_b32 s35, s34
	v_mul_f32_e32 v118, v117, v109
	ds_read_b64 v[0:1], v67 offset:10240
	ds_read_b64 v[2:3], v65 offset:10264
	ds_read_b64 v[4:5], v67 offset:10304
	ds_read_b64 v[6:7], v65 offset:10328
	ds_read_b64 v[8:9], v67 offset:12424
	ds_read_b64 v[10:11], v67 offset:12416
	ds_read_b64 v[12:13], v67 offset:12488
	ds_read_b64 v[14:15], v67 offset:12480
	ds_read_b64 v[16:17], v65 offset:14608
	ds_read_b64 v[18:19], v67 offset:14600
	ds_read_b64 v[20:21], v65 offset:14672
	ds_read_b64 v[22:23], v67 offset:14664
	ds_read_b64 v[24:25], v65 offset:16792
	ds_read_b64 v[26:27], v65 offset:16784
	ds_read_b64 v[28:29], v65 offset:16856
	ds_read_b64 v[30:31], v65 offset:16848
	s_waitcnt lgkmcnt(0)
	v_mov_b64_e32 v[88:89], s[32:33]
	v_mov_b64_e32 v[92:93], s[32:33]
	v_mov_b64_e32 v[96:97], s[32:33]
	v_mov_b64_e32 v[104:105], s[32:33]
	s_nop 1
	v_smfmac_f32_16x16x64_bf16 v[88:91], v[68:71], v[0:7], v64
	v_smfmac_f32_16x16x64_bf16 v[92:95], v[68:71], v[8:15], v64
	v_smfmac_f32_16x16x64_bf16 v[96:99], v[68:71], v[16:23], v64
	v_smfmac_f32_16x16x64_bf16 v[104:107], v[68:71], v[24:31], v64
	s_nop 4
	v_add_f32_dpp v108, v88, v89 quad_perm:[0,1,2,3] row_mask:0x1 bank_mask:0xf
	v_add_f32_dpp v108, v92, v93 quad_perm:[0,1,2,3] row_mask:0x2 bank_mask:0xf
	v_add_f32_dpp v108, v96, v97 quad_perm:[0,1,2,3] row_mask:0x4 bank_mask:0xf
	v_add_f32_dpp v108, v104, v105 quad_perm:[0,1,2,3] row_mask:0x8 bank_mask:0xf
	v_add_f32_e32 v108, 0xab8cbccc, v108
	v_mul_f32_e32 v108, v118, v108
	s_nop 1
	v_add_f32_dpp v108, v108, v108 row_ror:8 row_mask:0xf bank_mask:0xf
	s_nop 1
	v_add_f32_dpp v108, v108, v108 row_ror:4 row_mask:0xf bank_mask:0xf
	s_nop 1
	v_add_f32_dpp v108, v108, v108 row_ror:2 row_mask:0xf bank_mask:0xf
	s_nop 1
	v_add_f32_dpp v108, v108, v108 row_ror:1 row_mask:0xf bank_mask:0xf
	s_nop 1
	v_mov_b32_e32 v109, v108
	s_nop 1
	v_permlane16_swap_b32_e32 v108, v109
	v_add_f32_e32 v108, v108, v109
	v_mov_b32_e32 v109, v108
	s_nop 1
	v_permlane32_swap_b32_e32 v108, v109
	v_add_f32_e32 v108, v108, v109
	v_cmp_eq_u32_e32 vcc, 0, v100
	s_and_saveexec_b64 s[0:1], vcc
	s_cbranch_execz .LBB1_38
	s_mul_i32 s0, s22, 5
	s_add_i32 s0, s0, s23
	s_mov_b32 s1, 0
	s_lshl_b64 s[0:1], s[0:1], 2
	s_add_u32 s0, s12, s0
	s_addc_u32 s1, s13, s1
	v_mov_b32_e32 v109, 0
	global_store_dword v109, v108, s[0:1]
